# v43 with the whole instruction stream shifted by 4 bytes (one s_nop at entry): code-placement A/B (asm doc 9.3)
# speedup vs baseline: 1.0010x; 1.0010x over previous
; #define LAS __attribute__((address_space(3)))
; __device__ __forceinline__ unsigned xb_add(unsigned* p, unsigned v) { return __hip_atomic_fetch_add(p, v, __ATOMIC_RELAXED, __HIP_MEMORY_SCOPE_AGENT); }
; __device__ __forceinline__ unsigned xb_xcc_id() { return (unsigned)__builtin_amdgcn_s_getreg((3 << 11) | 20) & 0xFu; }
; __device__ __forceinline__ XcdBarrier xcd_barrier_post(unsigned* bar, volatile LAS unsigned* st) {
;     XcdBarrier b; b.bar = bar; b.x = xb_xcc_id(); b.st = st;
;     if (threadIdx.x == 0) (void)xb_add(&bar[XB_XCNT(b.x)], 1u);
;     return b;
; __global__ void __launch_bounds__(NTHREADS, 2) fwd(Args a) {
;     extern __shared__ __attribute__((aligned(16))) unsigned char lds_raw[];
;     LAS unsigned char* lds = (LAS unsigned char*)lds_raw;
;     (void)a;
;     if (threadIdx.x < 4) ((LAS unsigned*)(lds + LDS_BARW))[threadIdx.x] = 0u;
;     __syncthreads();
;     unsigned* ctl0 = (unsigned*)arg_ptr(30);
;     const XcdBarrier bar = xcd_barrier_post(ctl0 + CW_BAR, (volatile LAS unsigned*)(lds + LDS_BARW));
_Z3fwd4Args:
	s_nop 0
	s_mov_b32 s79, s2
	s_mov_b64 s[80:81], s[0:1]
	v_cmp_gt_u32_e32 vcc, 4, v0
	s_and_saveexec_b64 s[4:5], vcc
	v_lshl_add_u32 v1, v0, 2, 0
	v_add_u32_e32 v1, 0x26c00, v1
	v_mov_b32_e32 v2, 0
	ds_write_b32 v1, v2
	s_or_b64 exec, exec, s[4:5]
	s_mov_b32 s0, 30
	s_waitcnt lgkmcnt(0)
	s_barrier
	s_ashr_i32 s1, s0, 31
	s_lshl_b64 s[0:1], s[0:1], 3
	s_add_u32 s0, s80, s0
	s_addc_u32 s1, s81, s1
	s_load_dwordx2 s[0:1], s[0:1], 0x0
	s_mov_b32 s6, 30
	s_mov_b32 s4, 3
	s_waitcnt lgkmcnt(0)
	s_add_u32 s2, s0, 0x4000
	v_writelane_b32 v252, s0, 0
	s_addc_u32 s3, s1, 0
	s_nop 0
	v_writelane_b32 v252, s1, 1
	v_writelane_b32 v252, s2, 2
	s_getreg_b32 s0, hwreg(HW_REG_XCC_ID, 0, 4)
	s_and_b32 s0, s0, 15
	v_writelane_b32 v252, s3, 3
	v_writelane_b32 v252, s0, 4
	v_cmp_eq_u32_e64 s[0:1], 0, v0
	s_mov_b64 s[8:9], exec
	s_nop 0
	v_writelane_b32 v252, s0, 5
	s_nop 1
	v_writelane_b32 v252, s1, 6
	s_and_b64 s[0:1], s[8:9], s[0:1]
	s_mov_b64 exec, s[0:1]
	s_cbranch_execz .LBB0_5
	s_mov_b64 s[10:11], exec
	v_mbcnt_lo_u32_b32 v1, s10, 0
	v_mbcnt_hi_u32_b32 v1, s11, v1
	v_cmp_eq_u32_e32 vcc, 0, v1
	s_and_b64 s[0:1], exec, vcc
	s_mov_b64 exec, s[0:1]
	s_cbranch_execz .LBB0_5
	v_readlane_b32 s0, v252, 4
	s_lshl_b32 s0, s0, 8
	s_bcnt1_i32_b64 s1, s[10:11]
	v_mov_b32_e32 v1, s0
	v_mov_b32_e32 v2, s1
	v_readlane_b32 s0, v252, 2
	v_readlane_b32 s1, v252, 3
	s_nop 4
	global_atomic_add v1, v2, s[0:1] offset:1024
